# v26: v21 + grid barrier: top-generation polling, acquire issued at arrival, no wait for the XGEN atomic acknowledgement
# speedup vs baseline: 1.0061x; 1.0007x over previous
.LBB0_228:
	s_or_b64 exec, exec, s[6:7]
.LBB0_229:
	s_or_b64 exec, exec, s[2:3]
	s_waitcnt lgkmcnt(0)
	s_barrier

.LBB0_274:
	s_or_b64 exec, exec, s[4:5]
	v_cvt_f32_u32_e32 v5, v3
	s_waitcnt vmcnt(0)
	v_readfirstlane_b32 s0, v4
	v_sub_u32_e32 v4, 0, v3
	v_rcp_iflag_f32_e32 v5, v5
	v_add_u32_e32 v6, s0, v1
	v_mul_f32_e32 v5, 0x4f7ffffe, v5
	v_cvt_u32_f32_e32 v5, v5
	v_mul_lo_u32 v1, v4, v5
	v_mul_hi_u32 v1, v5, v1
	v_add_u32_e32 v1, v5, v1
	v_mul_hi_u32 v1, v6, v1
	v_mul_lo_u32 v4, v1, v3
	v_sub_u32_e32 v4, v6, v4
	v_add_u32_e32 v5, 1, v1
	v_cmp_ge_u32_e32 vcc, v4, v3
	s_nop 1
	v_cndmask_b32_e32 v1, v1, v5, vcc
	v_sub_u32_e32 v5, v4, v3
	v_cndmask_b32_e32 v4, v4, v5, vcc
	v_add_u32_e32 v5, 1, v1
	v_cmp_ge_u32_e32 vcc, v4, v3
	v_add_u32_e32 v4, 1, v6
	s_nop 0
	v_cndmask_b32_e32 v1, v1, v5, vcc
	v_mul_lo_u32 v5, v3, v1
	v_add_u32_e32 v3, v5, v3
	v_cmp_ne_u32_e32 vcc, v4, v3
	s_and_saveexec_b64 s[0:1], vcc
	s_xor_b64 s[4:5], exec, s[0:1]
	s_cbranch_execz .LBB0_288
	buffer_inv sc1
	s_getreg_b32 s0, hwreg(HW_REG_XCC_ID, 0, 4)
	s_lshl_b32 s0, s0, 8
	s_sub_u32 s0, 0x1100, s0
	v_mov_b32_e32 v5, s0
	v_readlane_b32 s0, v251, 17
	v_readlane_b32 s1, v251, 18
	s_waitcnt lgkmcnt(0)
	s_nop 3
	global_load_dword v2, v5, s[0:1] sc1
	s_waitcnt vmcnt(0)
	v_cmp_eq_u32_e32 vcc, v2, v1
	s_and_saveexec_b64 s[6:7], vcc
	s_cbranch_execz .LBB0_287
	s_mov_b32 s0, 1
	s_mov_b64 s[8:9], 0
	s_branch .LBB0_278

.LBB0_307:
	s_or_b64 exec, exec, s[6:7]
.LBB0_308:
	s_or_b64 exec, exec, s[2:3]
	v_readlane_b32 s4, v249, 15
	v_readlane_b32 s5, v249, 16
	s_waitcnt lgkmcnt(0)
	s_barrier

.LBB0_402:
	s_or_b64 exec, exec, s[4:5]
	v_cvt_f32_u32_e32 v5, v3
	s_waitcnt vmcnt(0)
	v_readfirstlane_b32 s1, v4
	v_sub_u32_e32 v4, 0, v3
	v_rcp_iflag_f32_e32 v5, v5
	v_add_u32_e32 v6, s1, v1
	v_mul_f32_e32 v5, 0x4f7ffffe, v5
	v_cvt_u32_f32_e32 v5, v5
	v_mul_lo_u32 v1, v4, v5
	v_mul_hi_u32 v1, v5, v1
	v_add_u32_e32 v1, v5, v1
	v_mul_hi_u32 v1, v6, v1
	v_mul_lo_u32 v4, v1, v3
	v_sub_u32_e32 v4, v6, v4
	v_add_u32_e32 v5, 1, v1
	v_cmp_ge_u32_e32 vcc, v4, v3
	s_nop 1
	v_cndmask_b32_e32 v1, v1, v5, vcc
	v_sub_u32_e32 v5, v4, v3
	v_cndmask_b32_e32 v4, v4, v5, vcc
	v_add_u32_e32 v5, 1, v1
	v_cmp_ge_u32_e32 vcc, v4, v3
	v_add_u32_e32 v4, 1, v6
	s_nop 0
	v_cndmask_b32_e32 v1, v1, v5, vcc
	v_mul_lo_u32 v5, v3, v1
	v_add_u32_e32 v3, v5, v3
	v_cmp_ne_u32_e32 vcc, v4, v3
	s_and_saveexec_b64 s[4:5], vcc
	s_xor_b64 s[4:5], exec, s[4:5]
	s_cbranch_execz .LBB0_416
	buffer_inv sc1
	s_getreg_b32 s6, hwreg(HW_REG_XCC_ID, 0, 4)
	s_lshl_b32 s6, s6, 8
	s_sub_u32 s6, 0x1100, s6
	v_mov_b32_e32 v5, s6
	v_readlane_b32 s6, v251, 17
	v_readlane_b32 s7, v251, 18
	s_waitcnt lgkmcnt(0)
	s_nop 3
	global_load_dword v2, v5, s[6:7] sc1
	s_waitcnt vmcnt(0)
	v_cmp_eq_u32_e32 vcc, v2, v1
	s_and_saveexec_b64 s[6:7], vcc
	s_cbranch_execz .LBB0_415
	s_mov_b32 s1, 1
	s_mov_b64 s[8:9], 0
	s_branch .LBB0_406

.LBB0_435:
	s_or_b64 exec, exec, s[6:7]
.LBB0_436:
	s_or_b64 exec, exec, s[2:3]
	s_waitcnt lgkmcnt(0)
	s_barrier

.LBB0_512:
	s_or_b64 exec, exec, s[4:5]
	v_cvt_f32_u32_e32 v5, v3
	s_waitcnt vmcnt(0)
	v_readfirstlane_b32 s0, v4
	v_sub_u32_e32 v4, 0, v3
	v_rcp_iflag_f32_e32 v5, v5
	v_add_u32_e32 v6, s0, v1
	v_mul_f32_e32 v5, 0x4f7ffffe, v5
	v_cvt_u32_f32_e32 v5, v5
	v_mul_lo_u32 v1, v4, v5
	v_mul_hi_u32 v1, v5, v1
	v_add_u32_e32 v1, v5, v1
	v_mul_hi_u32 v1, v6, v1
	v_mul_lo_u32 v4, v1, v3
	v_sub_u32_e32 v4, v6, v4
	v_add_u32_e32 v5, 1, v1
	v_cmp_ge_u32_e32 vcc, v4, v3
	s_nop 1
	v_cndmask_b32_e32 v1, v1, v5, vcc
	v_sub_u32_e32 v5, v4, v3
	v_cndmask_b32_e32 v4, v4, v5, vcc
	v_add_u32_e32 v5, 1, v1
	v_cmp_ge_u32_e32 vcc, v4, v3
	v_add_u32_e32 v4, 1, v6
	s_nop 0
	v_cndmask_b32_e32 v1, v1, v5, vcc
	v_mul_lo_u32 v5, v3, v1
	v_add_u32_e32 v3, v5, v3
	v_cmp_ne_u32_e32 vcc, v4, v3
	s_and_saveexec_b64 s[0:1], vcc
	s_xor_b64 s[4:5], exec, s[0:1]
	s_cbranch_execz .LBB0_526
	buffer_inv sc1
	s_getreg_b32 s0, hwreg(HW_REG_XCC_ID, 0, 4)
	s_lshl_b32 s0, s0, 8
	s_sub_u32 s0, 0x1100, s0
	v_mov_b32_e32 v5, s0
	v_readlane_b32 s0, v251, 17
	v_readlane_b32 s1, v251, 18
	s_waitcnt lgkmcnt(0)
	s_nop 3
	global_load_dword v2, v5, s[0:1] sc1
	s_waitcnt vmcnt(0)
	v_cmp_eq_u32_e32 vcc, v2, v1
	s_and_saveexec_b64 s[6:7], vcc
	s_cbranch_execz .LBB0_525
	s_mov_b32 s0, 1
	s_mov_b64 s[10:11], 0
	s_branch .LBB0_516

.LBB0_545:
	s_or_b64 exec, exec, s[6:7]
.LBB0_546:
	s_or_b64 exec, exec, s[2:3]
	s_waitcnt lgkmcnt(0)
	s_barrier
	s_mov_b64 s[6:7], -1

.LBB0_742:
	s_or_b64 exec, exec, s[4:5]
	v_cvt_f32_u32_e32 v5, v3
	s_waitcnt vmcnt(0)
	v_readfirstlane_b32 s1, v4
	v_sub_u32_e32 v4, 0, v3
	v_rcp_iflag_f32_e32 v5, v5
	v_add_u32_e32 v6, s1, v1
	v_mul_f32_e32 v5, 0x4f7ffffe, v5
	v_cvt_u32_f32_e32 v5, v5
	v_mul_lo_u32 v1, v4, v5
	v_mul_hi_u32 v1, v5, v1
	v_add_u32_e32 v1, v5, v1
	v_mul_hi_u32 v1, v6, v1
	v_mul_lo_u32 v4, v1, v3
	v_sub_u32_e32 v4, v6, v4
	v_add_u32_e32 v5, 1, v1
	v_cmp_ge_u32_e32 vcc, v4, v3
	s_nop 1
	v_cndmask_b32_e32 v1, v1, v5, vcc
	v_sub_u32_e32 v5, v4, v3
	v_cndmask_b32_e32 v4, v4, v5, vcc
	v_add_u32_e32 v5, 1, v1
	v_cmp_ge_u32_e32 vcc, v4, v3
	v_add_u32_e32 v4, 1, v6
	s_nop 0
	v_cndmask_b32_e32 v1, v1, v5, vcc
	v_mul_lo_u32 v5, v3, v1
	v_add_u32_e32 v3, v5, v3
	v_cmp_ne_u32_e32 vcc, v4, v3
	s_and_saveexec_b64 s[4:5], vcc
	s_xor_b64 s[4:5], exec, s[4:5]
	s_cbranch_execz .LBB0_756
	buffer_inv sc1
	s_getreg_b32 s8, hwreg(HW_REG_XCC_ID, 0, 4)
	s_lshl_b32 s8, s8, 8
	s_sub_u32 s8, 0x1100, s8
	v_mov_b32_e32 v5, s8
	v_readlane_b32 s8, v251, 17
	v_readlane_b32 s9, v251, 18
	s_waitcnt lgkmcnt(0)
	s_nop 3
	global_load_dword v2, v5, s[8:9] sc1
	s_waitcnt vmcnt(0)
	v_cmp_eq_u32_e32 vcc, v2, v1
	s_and_saveexec_b64 s[8:9], vcc
	s_cbranch_execz .LBB0_755
	s_mov_b32 s1, 1
	s_mov_b64 s[10:11], 0
	s_branch .LBB0_746

.LBB0_775:
	s_or_b64 exec, exec, s[8:9]
.LBB0_776:
	s_or_b64 exec, exec, s[2:3]
	s_waitcnt lgkmcnt(0)
	s_barrier

.LBB0_926:
	s_or_b64 exec, exec, s[8:9]
.LBB0_927:
	s_or_b64 exec, exec, s[2:3]
	s_waitcnt lgkmcnt(0)
	s_barrier

.LBB0_1145:
	s_or_b64 exec, exec, s[8:9]
.LBB0_1146:
	s_or_b64 exec, exec, s[2:3]
	s_waitcnt lgkmcnt(0)
	s_barrier

.LBB0_1236:
	s_or_b64 exec, exec, s[6:7]
.LBB0_1237:
	s_or_b64 exec, exec, s[2:3]
	s_waitcnt lgkmcnt(0)
	s_barrier
	s_mov_b64 s[6:7], -1

.LBB0_1375:
	s_or_b64 exec, exec, s[6:7]
.LBB0_1376:
	s_or_b64 exec, exec, s[2:3]
	s_waitcnt lgkmcnt(0)
	s_barrier

.LBB0_1698:
	s_or_b64 exec, exec, s[6:7]
.LBB0_1699:
	s_or_b64 exec, exec, s[2:3]
	s_waitcnt lgkmcnt(0)
	s_barrier

.LBB0_1701:
	s_or_b64 exec, exec, s[6:7]
.LBB0_1702:
	s_or_b64 exec, exec, s[2:3]
	s_waitcnt lgkmcnt(0)
	s_barrier

.LBB0_1755:
	s_or_b64 exec, exec, s[8:9]
	v_cvt_f32_u32_e32 v5, v3
	s_waitcnt vmcnt(0)
	v_readfirstlane_b32 s0, v4
	v_sub_u32_e32 v4, 0, v3
	v_rcp_iflag_f32_e32 v5, v5
	v_add_u32_e32 v6, s0, v1
	v_mul_f32_e32 v5, 0x4f7ffffe, v5
	v_cvt_u32_f32_e32 v5, v5
	v_mul_lo_u32 v1, v4, v5
	v_mul_hi_u32 v1, v5, v1
	v_add_u32_e32 v1, v5, v1
	v_mul_hi_u32 v1, v6, v1
	v_mul_lo_u32 v4, v1, v3
	v_sub_u32_e32 v4, v6, v4
	v_add_u32_e32 v5, 1, v1
	v_cmp_ge_u32_e32 vcc, v4, v3
	s_nop 1
	v_cndmask_b32_e32 v1, v1, v5, vcc
	v_sub_u32_e32 v5, v4, v3
	v_cndmask_b32_e32 v4, v4, v5, vcc
	v_add_u32_e32 v5, 1, v1
	v_cmp_ge_u32_e32 vcc, v4, v3
	v_add_u32_e32 v4, 1, v6
	s_nop 0
	v_cndmask_b32_e32 v1, v1, v5, vcc
	v_mul_lo_u32 v5, v3, v1
	v_add_u32_e32 v3, v5, v3
	v_cmp_ne_u32_e32 vcc, v4, v3
	s_and_saveexec_b64 s[0:1], vcc
	s_xor_b64 s[8:9], exec, s[0:1]
	s_cbranch_execz .LBB0_1769
	buffer_inv sc1
	s_getreg_b32 s0, hwreg(HW_REG_XCC_ID, 0, 4)
	s_lshl_b32 s0, s0, 8
	s_sub_u32 s0, 0x1100, s0
	v_mov_b32_e32 v5, s0
	v_readlane_b32 s0, v251, 17
	v_readlane_b32 s1, v251, 18
	s_waitcnt lgkmcnt(0)
	s_nop 3
	global_load_dword v2, v5, s[0:1] sc1
	s_waitcnt vmcnt(0)
	v_cmp_eq_u32_e32 vcc, v2, v1
	s_and_saveexec_b64 s[12:13], vcc
	s_cbranch_execz .LBB0_1768
	s_mov_b32 s0, 1
	s_mov_b64 s[22:23], 0
	s_branch .LBB0_1759

.LBB0_1788:
	s_or_b64 exec, exec, s[12:13]
.LBB0_1789:
	s_or_b64 exec, exec, s[2:3]
	v_readlane_b32 s8, v249, 15
	v_readlane_b32 s9, v249, 16
	s_waitcnt lgkmcnt(0)
	s_barrier

.LBB0_2018:
	s_or_b64 exec, exec, s[8:9]
.LBB0_2019:
	s_or_b64 exec, exec, s[2:3]
	s_waitcnt lgkmcnt(0)
	s_barrier
